# NSA QK^T K-fragment reads software-pipelined through free VGPRs, stacked on hoisted GEMM constants + unscaled fp8 MFMA + NSA mask
# baseline (speedup 1.0000x reference)
.LBB0_1732:
	v_bfe_u32 v1, v150, 1, 1
	v_cmp_ne_u32_e32 vcc, 0, v1
	s_cmp_lg_u64 vcc, 0
	s_cselect_b64 s[16:17], -1, 0
	s_cbranch_vccz .LBB0_1737
	ds_read_b128 v[212:215], v171 offset:49152
	ds_read_b128 v[216:219], v172 offset:49152
	ds_read_b128 v[220:223], v171 offset:57344
	ds_read_b128 v[224:227], v172 offset:57344
	ds_read_b128 v[228:231], v173 offset:49152
	ds_read_b128 v[232:235], v173 offset:57344
	ds_read_b128 v[236:239], v174 offset:49152
	ds_read_b128 v[240:243], v174 offset:57344
	ds_read_b128 v[244:247], v171 offset:49280
	ds_read_b128 v[248:251], v171 offset:57472
	s_cmp_eq_u32 s89, 1
	s_cselect_b64 s[14:15], -1, 0
	v_cndmask_b32_e64 v1, 64, v163, s[14:15]
	s_mov_b64 s[98:99], vcc
	v_cndmask_b32_e32 v1, 0, v1, vcc
	s_cmp_eq_u64 s[14:15], 0
	s_waitcnt lgkmcnt(9)
	v_mfma_f32_32x32x16_bf16 v[68:83], v[212:215], v[100:103], 0
	ds_read_b128 v[212:215], v172 offset:49280
	s_waitcnt lgkmcnt(9)
	v_mfma_f32_32x32x16_bf16 v[68:83], v[216:219], v[108:111], v[68:83]
	ds_read_b128 v[216:219], v172 offset:57472
	s_waitcnt lgkmcnt(9)
	v_mfma_f32_32x32x16_bf16 v[84:99], v[220:223], v[100:103], 0
	ds_read_b128 v[220:223], v173 offset:49280
	s_waitcnt lgkmcnt(9)
	v_mfma_f32_32x32x16_bf16 v[84:99], v[224:227], v[108:111], v[84:99]
	ds_read_b128 v[224:227], v173 offset:57472
	s_waitcnt lgkmcnt(9)
	v_mfma_f32_32x32x16_bf16 v[68:83], v[228:231], v[116:119], v[68:83]
	ds_read_b128 v[228:231], v174 offset:49280
	s_waitcnt lgkmcnt(9)
	v_mfma_f32_32x32x16_bf16 v[84:99], v[232:235], v[116:119], v[84:99]
	ds_read_b128 v[232:235], v174 offset:57472
	s_waitcnt lgkmcnt(9)
	v_mfma_f32_32x32x16_bf16 v[68:83], v[236:239], v[124:127], v[68:83]
	s_waitcnt lgkmcnt(8)
	v_mfma_f32_32x32x16_bf16 v[84:99], v[240:243], v[124:127], v[84:99]
	s_waitcnt lgkmcnt(7)
	v_mfma_f32_32x32x16_bf16 v[68:83], v[244:247], v[104:107], v[68:83]
	s_waitcnt lgkmcnt(6)
	v_mfma_f32_32x32x16_bf16 v[84:99], v[248:251], v[104:107], v[84:99]
	s_waitcnt lgkmcnt(5)
	v_mfma_f32_32x32x16_bf16 v[68:83], v[212:215], v[112:115], v[68:83]
	s_waitcnt lgkmcnt(4)
	v_mfma_f32_32x32x16_bf16 v[84:99], v[216:219], v[112:115], v[84:99]
	s_waitcnt lgkmcnt(3)
	v_mfma_f32_32x32x16_bf16 v[68:83], v[220:223], v[120:123], v[68:83]
	s_waitcnt lgkmcnt(2)
	v_mfma_f32_32x32x16_bf16 v[84:99], v[224:227], v[120:123], v[84:99]
	s_waitcnt lgkmcnt(1)
	v_mfma_f32_32x32x16_bf16 v[68:83], v[228:231], v[128:131], v[68:83]
	s_waitcnt lgkmcnt(0)
	s_nop 0
	v_mfma_f32_32x32x16_bf16 v[84:99], v[232:235], v[128:131], v[84:99]
	s_cbranch_scc1 .LBB0_1735
	v_sub_u32_e32 v1, v1, v137
	v_cmp_lt_i32_e32 vcc, 0, v1
	s_nop 5
	v_cndmask_b32_e32 v68, v168, v68, vcc
	v_cmp_lt_i32_e32 vcc, 32, v1
	s_nop 1
	v_cndmask_b32_e32 v84, v168, v84, vcc
	v_cmp_lt_i32_e32 vcc, 1, v1
	s_nop 1
	v_cndmask_b32_e32 v69, v168, v69, vcc
	v_cmp_lt_i32_e32 vcc, 33, v1
	s_nop 1
	v_cndmask_b32_e32 v85, v168, v85, vcc
	v_cmp_lt_i32_e32 vcc, 2, v1
	s_nop 1
	v_cndmask_b32_e32 v70, v168, v70, vcc
	v_cmp_lt_i32_e32 vcc, 34, v1
	s_nop 1
	v_cndmask_b32_e32 v86, v168, v86, vcc
	v_cmp_lt_i32_e32 vcc, 3, v1
	s_nop 1
	v_cndmask_b32_e32 v71, v168, v71, vcc
	v_cmp_lt_i32_e32 vcc, 35, v1
	s_nop 1
	v_cndmask_b32_e32 v87, v168, v87, vcc
	v_cmp_lt_i32_e32 vcc, 8, v1
	s_nop 1
	v_cndmask_b32_e32 v72, v168, v72, vcc
	v_cmp_lt_i32_e32 vcc, 40, v1
	s_nop 1
	v_cndmask_b32_e32 v88, v168, v88, vcc
	v_cmp_lt_i32_e32 vcc, 9, v1
	s_nop 1
	v_cndmask_b32_e32 v73, v168, v73, vcc
	v_cmp_lt_i32_e32 vcc, 41, v1
	s_nop 1
	v_cndmask_b32_e32 v89, v168, v89, vcc
	v_cmp_lt_i32_e32 vcc, 10, v1
	s_nop 1
	v_cndmask_b32_e32 v74, v168, v74, vcc
	v_cmp_lt_i32_e32 vcc, 42, v1
	s_nop 1
	v_cndmask_b32_e32 v90, v168, v90, vcc
	v_cmp_lt_i32_e32 vcc, 11, v1
	s_nop 1
	v_cndmask_b32_e32 v75, v168, v75, vcc
	v_cmp_lt_i32_e32 vcc, 43, v1
	s_nop 1
	v_cndmask_b32_e32 v91, v168, v91, vcc
	v_cmp_lt_i32_e32 vcc, 16, v1
	s_nop 1
	v_cndmask_b32_e32 v76, v168, v76, vcc
	v_cmp_lt_i32_e32 vcc, 48, v1
	s_nop 1
	v_cndmask_b32_e32 v92, v168, v92, vcc
	v_cmp_lt_i32_e32 vcc, 17, v1
	s_nop 1
	v_cndmask_b32_e32 v77, v168, v77, vcc
	v_cmp_lt_i32_e32 vcc, 49, v1
	s_nop 1
	v_cndmask_b32_e32 v93, v168, v93, vcc
	v_cmp_lt_i32_e32 vcc, 18, v1
	s_nop 1
	v_cndmask_b32_e32 v78, v168, v78, vcc
	v_cmp_lt_i32_e32 vcc, 50, v1
	s_nop 1
	v_cndmask_b32_e32 v94, v168, v94, vcc
	v_cmp_lt_i32_e32 vcc, 19, v1
	s_nop 1
	v_cndmask_b32_e32 v79, v168, v79, vcc
	v_cmp_lt_i32_e32 vcc, 51, v1
	s_nop 1
	v_cndmask_b32_e32 v95, v168, v95, vcc
	v_cmp_lt_i32_e32 vcc, 24, v1
	s_nop 1
	v_cndmask_b32_e32 v80, v168, v80, vcc
	v_cmp_lt_i32_e32 vcc, 56, v1
	s_nop 1
	v_cndmask_b32_e32 v96, v168, v96, vcc
	v_cmp_lt_i32_e32 vcc, 25, v1
	s_nop 1
	v_cndmask_b32_e32 v81, v168, v81, vcc
	v_cmp_lt_i32_e32 vcc, 57, v1
	s_nop 1
	v_cndmask_b32_e32 v97, v168, v97, vcc
	v_cmp_lt_i32_e32 vcc, 26, v1
	s_nop 1
	v_cndmask_b32_e32 v82, v168, v82, vcc
	v_cmp_lt_i32_e32 vcc, 58, v1
	s_nop 1
	v_cndmask_b32_e32 v98, v168, v98, vcc
	v_cmp_lt_i32_e32 vcc, 27, v1
	s_nop 1
	v_cndmask_b32_e32 v83, v168, v83, vcc
	v_cmp_lt_i32_e32 vcc, 59, v1
	s_nop 1
	v_cndmask_b32_e32 v99, v168, v99, vcc

.LBB0_1760:
	s_add_i32 s6, s1, s30
	s_cmp_lt_u32 s3, 32
	v_lshrrev_b32_e32 v1, s3, v150
	s_cselect_b64 s[12:13], -1, 0
	s_sub_i32 s3, s30, 35
	v_lshrrev_b32_e32 v2, s3, v151
	v_cndmask_b32_e64 v1, v2, v1, s[12:13]
	v_and_b32_e32 v1, 1, v1
	v_cmp_ne_u32_e32 vcc, 0, v1
	s_cmp_lg_u64 vcc, 0
	s_cselect_b64 s[20:21], -1, 0
	s_cbranch_vccz .LBB0_1765
	ds_read_b128 v[212:215], v171 offset:32768
	ds_read_b128 v[216:219], v172 offset:32768
	ds_read_b128 v[220:223], v171 offset:40960
	ds_read_b128 v[224:227], v172 offset:40960
	ds_read_b128 v[228:231], v173 offset:32768
	ds_read_b128 v[232:235], v173 offset:40960
	ds_read_b128 v[236:239], v174 offset:32768
	ds_read_b128 v[240:243], v174 offset:40960
	ds_read_b128 v[244:247], v171 offset:32896
	ds_read_b128 v[248:251], v171 offset:41088
	s_cmp_eq_u32 s6, 3
	s_cselect_b64 s[14:15], -1, 0
	v_cndmask_b32_e64 v1, 64, v163, s[14:15]
	s_mov_b64 s[98:99], vcc
	v_cndmask_b32_e32 v1, 0, v1, vcc
	s_cmp_eq_u64 s[14:15], 0
	s_waitcnt lgkmcnt(9)
	v_mfma_f32_32x32x16_bf16 v[68:83], v[212:215], v[100:103], 0
	ds_read_b128 v[212:215], v172 offset:32896
	s_waitcnt lgkmcnt(9)
	v_mfma_f32_32x32x16_bf16 v[68:83], v[216:219], v[108:111], v[68:83]
	ds_read_b128 v[216:219], v172 offset:41088
	s_waitcnt lgkmcnt(9)
	v_mfma_f32_32x32x16_bf16 v[84:99], v[220:223], v[100:103], 0
	ds_read_b128 v[220:223], v173 offset:32896
	s_waitcnt lgkmcnt(9)
	v_mfma_f32_32x32x16_bf16 v[84:99], v[224:227], v[108:111], v[84:99]
	ds_read_b128 v[224:227], v173 offset:41088
	s_waitcnt lgkmcnt(9)
	v_mfma_f32_32x32x16_bf16 v[68:83], v[228:231], v[116:119], v[68:83]
	ds_read_b128 v[228:231], v174 offset:32896
	s_waitcnt lgkmcnt(9)
	v_mfma_f32_32x32x16_bf16 v[84:99], v[232:235], v[116:119], v[84:99]
	ds_read_b128 v[232:235], v174 offset:41088
	s_waitcnt lgkmcnt(9)
	v_mfma_f32_32x32x16_bf16 v[68:83], v[236:239], v[124:127], v[68:83]
	s_waitcnt lgkmcnt(8)
	v_mfma_f32_32x32x16_bf16 v[84:99], v[240:243], v[124:127], v[84:99]
	s_waitcnt lgkmcnt(7)
	v_mfma_f32_32x32x16_bf16 v[68:83], v[244:247], v[104:107], v[68:83]
	s_waitcnt lgkmcnt(6)
	v_mfma_f32_32x32x16_bf16 v[84:99], v[248:251], v[104:107], v[84:99]
	s_waitcnt lgkmcnt(5)
	v_mfma_f32_32x32x16_bf16 v[68:83], v[212:215], v[112:115], v[68:83]
	s_waitcnt lgkmcnt(4)
	v_mfma_f32_32x32x16_bf16 v[84:99], v[216:219], v[112:115], v[84:99]
	s_waitcnt lgkmcnt(3)
	v_mfma_f32_32x32x16_bf16 v[68:83], v[220:223], v[120:123], v[68:83]
	s_waitcnt lgkmcnt(2)
	v_mfma_f32_32x32x16_bf16 v[84:99], v[224:227], v[120:123], v[84:99]
	s_waitcnt lgkmcnt(1)
	v_mfma_f32_32x32x16_bf16 v[68:83], v[228:231], v[128:131], v[68:83]
	s_waitcnt lgkmcnt(0)
	s_nop 0
	v_mfma_f32_32x32x16_bf16 v[84:99], v[232:235], v[128:131], v[84:99]
	s_cbranch_scc1 .LBB0_1763
	v_sub_u32_e32 v1, v1, v137
	v_cmp_lt_i32_e32 vcc, 0, v1
	s_nop 5
	v_cndmask_b32_e32 v68, v168, v68, vcc
	v_cmp_lt_i32_e32 vcc, 32, v1
	s_nop 1
	v_cndmask_b32_e32 v84, v168, v84, vcc
	v_cmp_lt_i32_e32 vcc, 1, v1
	s_nop 1
	v_cndmask_b32_e32 v69, v168, v69, vcc
	v_cmp_lt_i32_e32 vcc, 33, v1
	s_nop 1
	v_cndmask_b32_e32 v85, v168, v85, vcc
	v_cmp_lt_i32_e32 vcc, 2, v1
	s_nop 1
	v_cndmask_b32_e32 v70, v168, v70, vcc
	v_cmp_lt_i32_e32 vcc, 34, v1
	s_nop 1
	v_cndmask_b32_e32 v86, v168, v86, vcc
	v_cmp_lt_i32_e32 vcc, 3, v1
	s_nop 1
	v_cndmask_b32_e32 v71, v168, v71, vcc
	v_cmp_lt_i32_e32 vcc, 35, v1
	s_nop 1
	v_cndmask_b32_e32 v87, v168, v87, vcc
	v_cmp_lt_i32_e32 vcc, 8, v1
	s_nop 1
	v_cndmask_b32_e32 v72, v168, v72, vcc
	v_cmp_lt_i32_e32 vcc, 40, v1
	s_nop 1
	v_cndmask_b32_e32 v88, v168, v88, vcc
	v_cmp_lt_i32_e32 vcc, 9, v1
	s_nop 1
	v_cndmask_b32_e32 v73, v168, v73, vcc
	v_cmp_lt_i32_e32 vcc, 41, v1
	s_nop 1
	v_cndmask_b32_e32 v89, v168, v89, vcc
	v_cmp_lt_i32_e32 vcc, 10, v1
	s_nop 1
	v_cndmask_b32_e32 v74, v168, v74, vcc
	v_cmp_lt_i32_e32 vcc, 42, v1
	s_nop 1
	v_cndmask_b32_e32 v90, v168, v90, vcc
	v_cmp_lt_i32_e32 vcc, 11, v1
	s_nop 1
	v_cndmask_b32_e32 v75, v168, v75, vcc
	v_cmp_lt_i32_e32 vcc, 43, v1
	s_nop 1
	v_cndmask_b32_e32 v91, v168, v91, vcc
	v_cmp_lt_i32_e32 vcc, 16, v1
	s_nop 1
	v_cndmask_b32_e32 v76, v168, v76, vcc
	v_cmp_lt_i32_e32 vcc, 48, v1
	s_nop 1
	v_cndmask_b32_e32 v92, v168, v92, vcc
	v_cmp_lt_i32_e32 vcc, 17, v1
	s_nop 1
	v_cndmask_b32_e32 v77, v168, v77, vcc
	v_cmp_lt_i32_e32 vcc, 49, v1
	s_nop 1
	v_cndmask_b32_e32 v93, v168, v93, vcc
	v_cmp_lt_i32_e32 vcc, 18, v1
	s_nop 1
	v_cndmask_b32_e32 v78, v168, v78, vcc
	v_cmp_lt_i32_e32 vcc, 50, v1
	s_nop 1
	v_cndmask_b32_e32 v94, v168, v94, vcc
	v_cmp_lt_i32_e32 vcc, 19, v1
	s_nop 1
	v_cndmask_b32_e32 v79, v168, v79, vcc
	v_cmp_lt_i32_e32 vcc, 51, v1
	s_nop 1
	v_cndmask_b32_e32 v95, v168, v95, vcc
	v_cmp_lt_i32_e32 vcc, 24, v1
	s_nop 1
	v_cndmask_b32_e32 v80, v168, v80, vcc
	v_cmp_lt_i32_e32 vcc, 56, v1
	s_nop 1
	v_cndmask_b32_e32 v96, v168, v96, vcc
	v_cmp_lt_i32_e32 vcc, 25, v1
	s_nop 1
	v_cndmask_b32_e32 v81, v168, v81, vcc
	v_cmp_lt_i32_e32 vcc, 57, v1
	s_nop 1
	v_cndmask_b32_e32 v97, v168, v97, vcc
	v_cmp_lt_i32_e32 vcc, 26, v1
	s_nop 1
	v_cndmask_b32_e32 v82, v168, v82, vcc
	v_cmp_lt_i32_e32 vcc, 58, v1
	s_nop 1
	v_cndmask_b32_e32 v98, v168, v98, vcc
	v_cmp_lt_i32_e32 vcc, 27, v1
	s_nop 1
	v_cndmask_b32_e32 v83, v168, v83, vcc
	v_cmp_lt_i32_e32 vcc, 59, v1
	s_nop 1
	v_cndmask_b32_e32 v99, v168, v99, vcc

.LBB0_1784:
	s_add_i32 s4, s30, -2
	v_lshrrev_b32_e32 v1, s4, v150
	s_sub_i32 s4, s30, 34
	v_lshrrev_b32_e32 v2, s4, v151
	v_cndmask_b32_e64 v1, v2, v1, s[12:13]
	v_and_b32_e32 v1, 1, v1
	v_cmp_ne_u32_e32 vcc, 0, v1
	s_cmp_lg_u64 vcc, 0
	s_cselect_b64 s[16:17], -1, 0
	s_cbranch_vccz .LBB0_1789
	ds_read_b128 v[212:215], v171 offset:49152
	ds_read_b128 v[216:219], v172 offset:49152
	ds_read_b128 v[220:223], v171 offset:57344
	ds_read_b128 v[224:227], v172 offset:57344
	ds_read_b128 v[228:231], v173 offset:49152
	ds_read_b128 v[232:235], v173 offset:57344
	ds_read_b128 v[236:239], v174 offset:49152
	ds_read_b128 v[240:243], v174 offset:57344
	ds_read_b128 v[244:247], v171 offset:49280
	ds_read_b128 v[248:251], v171 offset:57472
	s_cmp_eq_u32 s6, 2
	s_cselect_b64 s[12:13], -1, 0
	v_cndmask_b32_e64 v1, 64, v163, s[12:13]
	s_mov_b64 s[98:99], vcc
	v_cndmask_b32_e32 v1, 0, v1, vcc
	s_cmp_eq_u64 s[12:13], 0
	s_waitcnt lgkmcnt(9)
	v_mfma_f32_32x32x16_bf16 v[68:83], v[212:215], v[100:103], 0
	ds_read_b128 v[212:215], v172 offset:49280
	s_waitcnt lgkmcnt(9)
	v_mfma_f32_32x32x16_bf16 v[68:83], v[216:219], v[108:111], v[68:83]
	ds_read_b128 v[216:219], v172 offset:57472
	s_waitcnt lgkmcnt(9)
	v_mfma_f32_32x32x16_bf16 v[84:99], v[220:223], v[100:103], 0
	ds_read_b128 v[220:223], v173 offset:49280
	s_waitcnt lgkmcnt(9)
	v_mfma_f32_32x32x16_bf16 v[84:99], v[224:227], v[108:111], v[84:99]
	ds_read_b128 v[224:227], v173 offset:57472
	s_waitcnt lgkmcnt(9)
	v_mfma_f32_32x32x16_bf16 v[68:83], v[228:231], v[116:119], v[68:83]
	ds_read_b128 v[228:231], v174 offset:49280
	s_waitcnt lgkmcnt(9)
	v_mfma_f32_32x32x16_bf16 v[84:99], v[232:235], v[116:119], v[84:99]
	ds_read_b128 v[232:235], v174 offset:57472
	s_waitcnt lgkmcnt(9)
	v_mfma_f32_32x32x16_bf16 v[68:83], v[236:239], v[124:127], v[68:83]
	s_waitcnt lgkmcnt(8)
	v_mfma_f32_32x32x16_bf16 v[84:99], v[240:243], v[124:127], v[84:99]
	s_waitcnt lgkmcnt(7)
	v_mfma_f32_32x32x16_bf16 v[68:83], v[244:247], v[104:107], v[68:83]
	s_waitcnt lgkmcnt(6)
	v_mfma_f32_32x32x16_bf16 v[84:99], v[248:251], v[104:107], v[84:99]
	s_waitcnt lgkmcnt(5)
	v_mfma_f32_32x32x16_bf16 v[68:83], v[212:215], v[112:115], v[68:83]
	s_waitcnt lgkmcnt(4)
	v_mfma_f32_32x32x16_bf16 v[84:99], v[216:219], v[112:115], v[84:99]
	s_waitcnt lgkmcnt(3)
	v_mfma_f32_32x32x16_bf16 v[68:83], v[220:223], v[120:123], v[68:83]
	s_waitcnt lgkmcnt(2)
	v_mfma_f32_32x32x16_bf16 v[84:99], v[224:227], v[120:123], v[84:99]
	s_waitcnt lgkmcnt(1)
	v_mfma_f32_32x32x16_bf16 v[68:83], v[228:231], v[128:131], v[68:83]
	s_waitcnt lgkmcnt(0)
	s_nop 0
	v_mfma_f32_32x32x16_bf16 v[84:99], v[232:235], v[128:131], v[84:99]
	s_cbranch_scc1 .LBB0_1787
	v_sub_u32_e32 v1, v1, v137
	v_cmp_lt_i32_e32 vcc, 0, v1
	s_nop 5
	v_cndmask_b32_e32 v68, v168, v68, vcc
	v_cmp_lt_i32_e32 vcc, 32, v1
	s_nop 1
	v_cndmask_b32_e32 v84, v168, v84, vcc
	v_cmp_lt_i32_e32 vcc, 1, v1
	s_nop 1
	v_cndmask_b32_e32 v69, v168, v69, vcc
	v_cmp_lt_i32_e32 vcc, 33, v1
	s_nop 1
	v_cndmask_b32_e32 v85, v168, v85, vcc
	v_cmp_lt_i32_e32 vcc, 2, v1
	s_nop 1
	v_cndmask_b32_e32 v70, v168, v70, vcc
	v_cmp_lt_i32_e32 vcc, 34, v1
	s_nop 1
	v_cndmask_b32_e32 v86, v168, v86, vcc
	v_cmp_lt_i32_e32 vcc, 3, v1
	s_nop 1
	v_cndmask_b32_e32 v71, v168, v71, vcc
	v_cmp_lt_i32_e32 vcc, 35, v1
	s_nop 1
	v_cndmask_b32_e32 v87, v168, v87, vcc
	v_cmp_lt_i32_e32 vcc, 8, v1
	s_nop 1
	v_cndmask_b32_e32 v72, v168, v72, vcc
	v_cmp_lt_i32_e32 vcc, 40, v1
	s_nop 1
	v_cndmask_b32_e32 v88, v168, v88, vcc
	v_cmp_lt_i32_e32 vcc, 9, v1
	s_nop 1
	v_cndmask_b32_e32 v73, v168, v73, vcc
	v_cmp_lt_i32_e32 vcc, 41, v1
	s_nop 1
	v_cndmask_b32_e32 v89, v168, v89, vcc
	v_cmp_lt_i32_e32 vcc, 10, v1
	s_nop 1
	v_cndmask_b32_e32 v74, v168, v74, vcc
	v_cmp_lt_i32_e32 vcc, 42, v1
	s_nop 1
	v_cndmask_b32_e32 v90, v168, v90, vcc
	v_cmp_lt_i32_e32 vcc, 11, v1
	s_nop 1
	v_cndmask_b32_e32 v75, v168, v75, vcc
	v_cmp_lt_i32_e32 vcc, 43, v1
	s_nop 1
	v_cndmask_b32_e32 v91, v168, v91, vcc
	v_cmp_lt_i32_e32 vcc, 16, v1
	s_nop 1
	v_cndmask_b32_e32 v76, v168, v76, vcc
	v_cmp_lt_i32_e32 vcc, 48, v1
	s_nop 1
	v_cndmask_b32_e32 v92, v168, v92, vcc
	v_cmp_lt_i32_e32 vcc, 17, v1
	s_nop 1
	v_cndmask_b32_e32 v77, v168, v77, vcc
	v_cmp_lt_i32_e32 vcc, 49, v1
	s_nop 1
	v_cndmask_b32_e32 v93, v168, v93, vcc
	v_cmp_lt_i32_e32 vcc, 18, v1
	s_nop 1
	v_cndmask_b32_e32 v78, v168, v78, vcc
	v_cmp_lt_i32_e32 vcc, 50, v1
	s_nop 1
	v_cndmask_b32_e32 v94, v168, v94, vcc
	v_cmp_lt_i32_e32 vcc, 19, v1
	s_nop 1
	v_cndmask_b32_e32 v79, v168, v79, vcc
	v_cmp_lt_i32_e32 vcc, 51, v1
	s_nop 1
	v_cndmask_b32_e32 v95, v168, v95, vcc
	v_cmp_lt_i32_e32 vcc, 24, v1
	s_nop 1
	v_cndmask_b32_e32 v80, v168, v80, vcc
	v_cmp_lt_i32_e32 vcc, 56, v1
	s_nop 1
	v_cndmask_b32_e32 v96, v168, v96, vcc
	v_cmp_lt_i32_e32 vcc, 25, v1
	s_nop 1
	v_cndmask_b32_e32 v81, v168, v81, vcc
	v_cmp_lt_i32_e32 vcc, 57, v1
	s_nop 1
	v_cndmask_b32_e32 v97, v168, v97, vcc
	v_cmp_lt_i32_e32 vcc, 26, v1
	s_nop 1
	v_cndmask_b32_e32 v82, v168, v82, vcc
	v_cmp_lt_i32_e32 vcc, 58, v1
	s_nop 1
	v_cndmask_b32_e32 v98, v168, v98, vcc
	v_cmp_lt_i32_e32 vcc, 27, v1
	s_nop 1
	v_cndmask_b32_e32 v83, v168, v83, vcc
	v_cmp_lt_i32_e32 vcc, 59, v1
	s_nop 1
	v_cndmask_b32_e32 v99, v168, v99, vcc

.LBB0_1827:
	v_bfe_u32 v1, v150, 1, 1
	v_cmp_ne_u32_e32 vcc, 0, v1
	s_cmp_lg_u64 vcc, 0
	s_cselect_b64 s[12:13], -1, 0
	s_cbranch_vccz .LBB0_1832
	ds_read_b128 v[212:215], v142 offset:49152
	ds_read_b128 v[216:219], v143 offset:49152
	ds_read_b128 v[220:223], v142 offset:57344
	ds_read_b128 v[224:227], v143 offset:57344
	ds_read_b128 v[228:231], v152 offset:49152
	ds_read_b128 v[232:235], v152 offset:57344
	ds_read_b128 v[236:239], v153 offset:49152
	ds_read_b128 v[240:243], v153 offset:57344
	ds_read_b128 v[244:247], v142 offset:49280
	ds_read_b128 v[248:251], v142 offset:57472
	v_cndmask_b32_e64 v1, 64, v163, s[10:11]
	s_mov_b64 s[98:99], vcc
	v_cndmask_b32_e32 v1, 0, v1, vcc
	s_cmp_eq_u64 s[10:11], 0
	s_waitcnt lgkmcnt(9)
	v_mfma_f32_32x32x16_bf16 v[68:83], v[212:215], v[100:103], 0
	ds_read_b128 v[212:215], v143 offset:49280
	s_waitcnt lgkmcnt(9)
	v_mfma_f32_32x32x16_bf16 v[68:83], v[216:219], v[108:111], v[68:83]
	ds_read_b128 v[216:219], v143 offset:57472
	s_waitcnt lgkmcnt(9)
	v_mfma_f32_32x32x16_bf16 v[84:99], v[220:223], v[100:103], 0
	ds_read_b128 v[220:223], v152 offset:49280
	s_waitcnt lgkmcnt(9)
	v_mfma_f32_32x32x16_bf16 v[84:99], v[224:227], v[108:111], v[84:99]
	ds_read_b128 v[224:227], v152 offset:57472
	s_waitcnt lgkmcnt(9)
	v_mfma_f32_32x32x16_bf16 v[68:83], v[228:231], v[116:119], v[68:83]
	ds_read_b128 v[228:231], v153 offset:49280
	s_waitcnt lgkmcnt(9)
	v_mfma_f32_32x32x16_bf16 v[84:99], v[232:235], v[116:119], v[84:99]
	ds_read_b128 v[232:235], v153 offset:57472
	s_waitcnt lgkmcnt(9)
	v_mfma_f32_32x32x16_bf16 v[68:83], v[236:239], v[124:127], v[68:83]
	s_waitcnt lgkmcnt(8)
	v_mfma_f32_32x32x16_bf16 v[84:99], v[240:243], v[124:127], v[84:99]
	s_waitcnt lgkmcnt(7)
	v_mfma_f32_32x32x16_bf16 v[68:83], v[244:247], v[104:107], v[68:83]
	s_waitcnt lgkmcnt(6)
	v_mfma_f32_32x32x16_bf16 v[84:99], v[248:251], v[104:107], v[84:99]
	s_waitcnt lgkmcnt(5)
	v_mfma_f32_32x32x16_bf16 v[68:83], v[212:215], v[112:115], v[68:83]
	s_waitcnt lgkmcnt(4)
	v_mfma_f32_32x32x16_bf16 v[84:99], v[216:219], v[112:115], v[84:99]
	s_waitcnt lgkmcnt(3)
	v_mfma_f32_32x32x16_bf16 v[68:83], v[220:223], v[120:123], v[68:83]
	s_waitcnt lgkmcnt(2)
	v_mfma_f32_32x32x16_bf16 v[84:99], v[224:227], v[120:123], v[84:99]
	s_waitcnt lgkmcnt(1)
	v_mfma_f32_32x32x16_bf16 v[68:83], v[228:231], v[128:131], v[68:83]
	s_waitcnt lgkmcnt(0)
	s_nop 0
	v_mfma_f32_32x32x16_bf16 v[84:99], v[232:235], v[128:131], v[84:99]
	s_cbranch_scc1 .LBB0_1830
	v_sub_u32_e32 v1, v1, v137
	v_cmp_lt_i32_e32 vcc, 0, v1
	s_nop 5
	v_cndmask_b32_e32 v68, v168, v68, vcc
	v_cmp_lt_i32_e32 vcc, 32, v1
	s_nop 1
	v_cndmask_b32_e32 v84, v168, v84, vcc
	v_cmp_lt_i32_e32 vcc, 1, v1
	s_nop 1
	v_cndmask_b32_e32 v69, v168, v69, vcc
	v_cmp_lt_i32_e32 vcc, 33, v1
	s_nop 1
	v_cndmask_b32_e32 v85, v168, v85, vcc
	v_cmp_lt_i32_e32 vcc, 2, v1
	s_nop 1
	v_cndmask_b32_e32 v70, v168, v70, vcc
	v_cmp_lt_i32_e32 vcc, 34, v1
	s_nop 1
	v_cndmask_b32_e32 v86, v168, v86, vcc
	v_cmp_lt_i32_e32 vcc, 3, v1
	s_nop 1
	v_cndmask_b32_e32 v71, v168, v71, vcc
	v_cmp_lt_i32_e32 vcc, 35, v1
	s_nop 1
	v_cndmask_b32_e32 v87, v168, v87, vcc
	v_cmp_lt_i32_e32 vcc, 8, v1
	s_nop 1
	v_cndmask_b32_e32 v72, v168, v72, vcc
	v_cmp_lt_i32_e32 vcc, 40, v1
	s_nop 1
	v_cndmask_b32_e32 v88, v168, v88, vcc
	v_cmp_lt_i32_e32 vcc, 9, v1
	s_nop 1
	v_cndmask_b32_e32 v73, v168, v73, vcc
	v_cmp_lt_i32_e32 vcc, 41, v1
	s_nop 1
	v_cndmask_b32_e32 v89, v168, v89, vcc
	v_cmp_lt_i32_e32 vcc, 10, v1
	s_nop 1
	v_cndmask_b32_e32 v74, v168, v74, vcc
	v_cmp_lt_i32_e32 vcc, 42, v1
	s_nop 1
	v_cndmask_b32_e32 v90, v168, v90, vcc
	v_cmp_lt_i32_e32 vcc, 11, v1
	s_nop 1
	v_cndmask_b32_e32 v75, v168, v75, vcc
	v_cmp_lt_i32_e32 vcc, 43, v1
	s_nop 1
	v_cndmask_b32_e32 v91, v168, v91, vcc
	v_cmp_lt_i32_e32 vcc, 16, v1
	s_nop 1
	v_cndmask_b32_e32 v76, v168, v76, vcc
	v_cmp_lt_i32_e32 vcc, 48, v1
	s_nop 1
	v_cndmask_b32_e32 v92, v168, v92, vcc
	v_cmp_lt_i32_e32 vcc, 17, v1
	s_nop 1
	v_cndmask_b32_e32 v77, v168, v77, vcc
	v_cmp_lt_i32_e32 vcc, 49, v1
	s_nop 1
	v_cndmask_b32_e32 v93, v168, v93, vcc
	v_cmp_lt_i32_e32 vcc, 18, v1
	s_nop 1
	v_cndmask_b32_e32 v78, v168, v78, vcc
	v_cmp_lt_i32_e32 vcc, 50, v1
	s_nop 1
	v_cndmask_b32_e32 v94, v168, v94, vcc
	v_cmp_lt_i32_e32 vcc, 19, v1
	s_nop 1
	v_cndmask_b32_e32 v79, v168, v79, vcc
	v_cmp_lt_i32_e32 vcc, 51, v1
	s_nop 1
	v_cndmask_b32_e32 v95, v168, v95, vcc
	v_cmp_lt_i32_e32 vcc, 24, v1
	s_nop 1
	v_cndmask_b32_e32 v80, v168, v80, vcc
	v_cmp_lt_i32_e32 vcc, 56, v1
	s_nop 1
	v_cndmask_b32_e32 v96, v168, v96, vcc
	v_cmp_lt_i32_e32 vcc, 25, v1
	s_nop 1
	v_cndmask_b32_e32 v81, v168, v81, vcc
	v_cmp_lt_i32_e32 vcc, 57, v1
	s_nop 1
	v_cndmask_b32_e32 v97, v168, v97, vcc
	v_cmp_lt_i32_e32 vcc, 26, v1
	s_nop 1
	v_cndmask_b32_e32 v82, v168, v82, vcc
	v_cmp_lt_i32_e32 vcc, 58, v1
	s_nop 1
	v_cndmask_b32_e32 v98, v168, v98, vcc
	v_cmp_lt_i32_e32 vcc, 27, v1
	s_nop 1
	v_cndmask_b32_e32 v83, v168, v83, vcc
	v_cmp_lt_i32_e32 vcc, 59, v1
	s_nop 1
	v_cndmask_b32_e32 v99, v168, v99, vcc

.LBB0_1853:
	s_add_i32 s3, s1, s28
	s_cmp_lt_u32 s4, 32
	v_lshrrev_b32_e32 v1, s4, v150
	s_cselect_b64 s[10:11], -1, 0
	s_sub_i32 s4, s28, 34
	v_lshrrev_b32_e32 v2, s4, v151
	v_cndmask_b32_e64 v1, v2, v1, s[10:11]
	v_and_b32_e32 v1, 1, v1
	v_cmp_ne_u32_e32 vcc, 0, v1
	s_cmp_lg_u64 vcc, 0
	s_cselect_b64 s[18:19], -1, 0
	s_cbranch_vccz .LBB0_1858
	ds_read_b128 v[212:215], v142 offset:32768
	ds_read_b128 v[216:219], v143 offset:32768
	ds_read_b128 v[220:223], v142 offset:40960
	ds_read_b128 v[224:227], v143 offset:40960
	ds_read_b128 v[228:231], v152 offset:32768
	ds_read_b128 v[232:235], v152 offset:40960
	ds_read_b128 v[236:239], v153 offset:32768
	ds_read_b128 v[240:243], v153 offset:40960
	ds_read_b128 v[244:247], v142 offset:32896
	ds_read_b128 v[248:251], v142 offset:41088
	s_cmp_eq_u32 s3, 2
	s_cselect_b64 s[12:13], -1, 0
	v_cndmask_b32_e64 v1, 64, v163, s[12:13]
	s_mov_b64 s[98:99], vcc
	v_cndmask_b32_e32 v1, 0, v1, vcc
	s_cmp_eq_u64 s[12:13], 0
	s_waitcnt lgkmcnt(9)
	v_mfma_f32_32x32x16_bf16 v[68:83], v[212:215], v[100:103], 0
	ds_read_b128 v[212:215], v143 offset:32896
	s_waitcnt lgkmcnt(9)
	v_mfma_f32_32x32x16_bf16 v[68:83], v[216:219], v[108:111], v[68:83]
	ds_read_b128 v[216:219], v143 offset:41088
	s_waitcnt lgkmcnt(9)
	v_mfma_f32_32x32x16_bf16 v[84:99], v[220:223], v[100:103], 0
	ds_read_b128 v[220:223], v152 offset:32896
	s_waitcnt lgkmcnt(9)
	v_mfma_f32_32x32x16_bf16 v[84:99], v[224:227], v[108:111], v[84:99]
	ds_read_b128 v[224:227], v152 offset:41088
	s_waitcnt lgkmcnt(9)
	v_mfma_f32_32x32x16_bf16 v[68:83], v[228:231], v[116:119], v[68:83]
	ds_read_b128 v[228:231], v153 offset:32896
	s_waitcnt lgkmcnt(9)
	v_mfma_f32_32x32x16_bf16 v[84:99], v[232:235], v[116:119], v[84:99]
	ds_read_b128 v[232:235], v153 offset:41088
	s_waitcnt lgkmcnt(9)
	v_mfma_f32_32x32x16_bf16 v[68:83], v[236:239], v[124:127], v[68:83]
	s_waitcnt lgkmcnt(8)
	v_mfma_f32_32x32x16_bf16 v[84:99], v[240:243], v[124:127], v[84:99]
	s_waitcnt lgkmcnt(7)
	v_mfma_f32_32x32x16_bf16 v[68:83], v[244:247], v[104:107], v[68:83]
	s_waitcnt lgkmcnt(6)
	v_mfma_f32_32x32x16_bf16 v[84:99], v[248:251], v[104:107], v[84:99]
	s_waitcnt lgkmcnt(5)
	v_mfma_f32_32x32x16_bf16 v[68:83], v[212:215], v[112:115], v[68:83]
	s_waitcnt lgkmcnt(4)
	v_mfma_f32_32x32x16_bf16 v[84:99], v[216:219], v[112:115], v[84:99]
	s_waitcnt lgkmcnt(3)
	v_mfma_f32_32x32x16_bf16 v[68:83], v[220:223], v[120:123], v[68:83]
	s_waitcnt lgkmcnt(2)
	v_mfma_f32_32x32x16_bf16 v[84:99], v[224:227], v[120:123], v[84:99]
	s_waitcnt lgkmcnt(1)
	v_mfma_f32_32x32x16_bf16 v[68:83], v[228:231], v[128:131], v[68:83]
	s_waitcnt lgkmcnt(0)
	s_nop 0
	v_mfma_f32_32x32x16_bf16 v[84:99], v[232:235], v[128:131], v[84:99]
	s_cbranch_scc1 .LBB0_1856
	v_sub_u32_e32 v1, v1, v137
	v_cmp_lt_i32_e32 vcc, 0, v1
	s_nop 5
	v_cndmask_b32_e32 v68, v168, v68, vcc
	v_cmp_lt_i32_e32 vcc, 32, v1
	s_nop 1
	v_cndmask_b32_e32 v84, v168, v84, vcc
	v_cmp_lt_i32_e32 vcc, 1, v1
	s_nop 1
	v_cndmask_b32_e32 v69, v168, v69, vcc
	v_cmp_lt_i32_e32 vcc, 33, v1
	s_nop 1
	v_cndmask_b32_e32 v85, v168, v85, vcc
	v_cmp_lt_i32_e32 vcc, 2, v1
	s_nop 1
	v_cndmask_b32_e32 v70, v168, v70, vcc
	v_cmp_lt_i32_e32 vcc, 34, v1
	s_nop 1
	v_cndmask_b32_e32 v86, v168, v86, vcc
	v_cmp_lt_i32_e32 vcc, 3, v1
	s_nop 1
	v_cndmask_b32_e32 v71, v168, v71, vcc
	v_cmp_lt_i32_e32 vcc, 35, v1
	s_nop 1
	v_cndmask_b32_e32 v87, v168, v87, vcc
	v_cmp_lt_i32_e32 vcc, 8, v1
	s_nop 1
	v_cndmask_b32_e32 v72, v168, v72, vcc
	v_cmp_lt_i32_e32 vcc, 40, v1
	s_nop 1
	v_cndmask_b32_e32 v88, v168, v88, vcc
	v_cmp_lt_i32_e32 vcc, 9, v1
	s_nop 1
	v_cndmask_b32_e32 v73, v168, v73, vcc
	v_cmp_lt_i32_e32 vcc, 41, v1
	s_nop 1
	v_cndmask_b32_e32 v89, v168, v89, vcc
	v_cmp_lt_i32_e32 vcc, 10, v1
	s_nop 1
	v_cndmask_b32_e32 v74, v168, v74, vcc
	v_cmp_lt_i32_e32 vcc, 42, v1
	s_nop 1
	v_cndmask_b32_e32 v90, v168, v90, vcc
	v_cmp_lt_i32_e32 vcc, 11, v1
	s_nop 1
	v_cndmask_b32_e32 v75, v168, v75, vcc
	v_cmp_lt_i32_e32 vcc, 43, v1
	s_nop 1
	v_cndmask_b32_e32 v91, v168, v91, vcc
	v_cmp_lt_i32_e32 vcc, 16, v1
	s_nop 1
	v_cndmask_b32_e32 v76, v168, v76, vcc
	v_cmp_lt_i32_e32 vcc, 48, v1
	s_nop 1
	v_cndmask_b32_e32 v92, v168, v92, vcc
	v_cmp_lt_i32_e32 vcc, 17, v1
	s_nop 1
	v_cndmask_b32_e32 v77, v168, v77, vcc
	v_cmp_lt_i32_e32 vcc, 49, v1
	s_nop 1
	v_cndmask_b32_e32 v93, v168, v93, vcc
	v_cmp_lt_i32_e32 vcc, 18, v1
	s_nop 1
	v_cndmask_b32_e32 v78, v168, v78, vcc
	v_cmp_lt_i32_e32 vcc, 50, v1
	s_nop 1
	v_cndmask_b32_e32 v94, v168, v94, vcc
	v_cmp_lt_i32_e32 vcc, 19, v1
	s_nop 1
	v_cndmask_b32_e32 v79, v168, v79, vcc
	v_cmp_lt_i32_e32 vcc, 51, v1
	s_nop 1
	v_cndmask_b32_e32 v95, v168, v95, vcc
	v_cmp_lt_i32_e32 vcc, 24, v1
	s_nop 1
	v_cndmask_b32_e32 v80, v168, v80, vcc
	v_cmp_lt_i32_e32 vcc, 56, v1
	s_nop 1
	v_cndmask_b32_e32 v96, v168, v96, vcc
	v_cmp_lt_i32_e32 vcc, 25, v1
	s_nop 1
	v_cndmask_b32_e32 v81, v168, v81, vcc
	v_cmp_lt_i32_e32 vcc, 57, v1
	s_nop 1
	v_cndmask_b32_e32 v97, v168, v97, vcc
	v_cmp_lt_i32_e32 vcc, 26, v1
	s_nop 1
	v_cndmask_b32_e32 v82, v168, v82, vcc
	v_cmp_lt_i32_e32 vcc, 58, v1
	s_nop 1
	v_cndmask_b32_e32 v98, v168, v98, vcc
	v_cmp_lt_i32_e32 vcc, 27, v1
	s_nop 1
	v_cndmask_b32_e32 v83, v168, v83, vcc
	v_cmp_lt_i32_e32 vcc, 59, v1
	s_nop 1
	v_cndmask_b32_e32 v99, v168, v99, vcc

.LBB0_1877:
	s_add_i32 s4, s28, -1
	v_lshrrev_b32_e32 v1, s4, v150
	s_sub_i32 s4, s28, 33
	v_lshrrev_b32_e32 v2, s4, v151
	v_cndmask_b32_e64 v1, v2, v1, s[10:11]
	v_and_b32_e32 v1, 1, v1
	v_cmp_ne_u32_e32 vcc, 0, v1
	s_cmp_lg_u64 vcc, 0
	s_cselect_b64 s[12:13], -1, 0
	s_cbranch_vccz .LBB0_1882
	ds_read_b128 v[212:215], v142 offset:49152
	ds_read_b128 v[216:219], v143 offset:49152
	ds_read_b128 v[220:223], v142 offset:57344
	ds_read_b128 v[224:227], v143 offset:57344
	ds_read_b128 v[228:231], v152 offset:49152
	ds_read_b128 v[232:235], v152 offset:57344
	ds_read_b128 v[236:239], v153 offset:49152
	ds_read_b128 v[240:243], v153 offset:57344
	ds_read_b128 v[244:247], v142 offset:49280
	ds_read_b128 v[248:251], v142 offset:57472
	s_cmp_eq_u32 s3, 1
	s_cselect_b64 s[10:11], -1, 0
	v_cndmask_b32_e64 v1, 64, v163, s[10:11]
	s_mov_b64 s[98:99], vcc
	v_cndmask_b32_e32 v1, 0, v1, vcc
	s_cmp_eq_u64 s[10:11], 0
	s_waitcnt lgkmcnt(9)
	v_mfma_f32_32x32x16_bf16 v[68:83], v[212:215], v[100:103], 0
	ds_read_b128 v[212:215], v143 offset:49280
	s_waitcnt lgkmcnt(9)
	v_mfma_f32_32x32x16_bf16 v[68:83], v[216:219], v[108:111], v[68:83]
	ds_read_b128 v[216:219], v143 offset:57472
	s_waitcnt lgkmcnt(9)
	v_mfma_f32_32x32x16_bf16 v[84:99], v[220:223], v[100:103], 0
	ds_read_b128 v[220:223], v152 offset:49280
	s_waitcnt lgkmcnt(9)
	v_mfma_f32_32x32x16_bf16 v[84:99], v[224:227], v[108:111], v[84:99]
	ds_read_b128 v[224:227], v152 offset:57472
	s_waitcnt lgkmcnt(9)
	v_mfma_f32_32x32x16_bf16 v[68:83], v[228:231], v[116:119], v[68:83]
	ds_read_b128 v[228:231], v153 offset:49280
	s_waitcnt lgkmcnt(9)
	v_mfma_f32_32x32x16_bf16 v[84:99], v[232:235], v[116:119], v[84:99]
	ds_read_b128 v[232:235], v153 offset:57472
	s_waitcnt lgkmcnt(9)
	v_mfma_f32_32x32x16_bf16 v[68:83], v[236:239], v[124:127], v[68:83]
	s_waitcnt lgkmcnt(8)
	v_mfma_f32_32x32x16_bf16 v[84:99], v[240:243], v[124:127], v[84:99]
	s_waitcnt lgkmcnt(7)
	v_mfma_f32_32x32x16_bf16 v[68:83], v[244:247], v[104:107], v[68:83]
	s_waitcnt lgkmcnt(6)
	v_mfma_f32_32x32x16_bf16 v[84:99], v[248:251], v[104:107], v[84:99]
	s_waitcnt lgkmcnt(5)
	v_mfma_f32_32x32x16_bf16 v[68:83], v[212:215], v[112:115], v[68:83]
	s_waitcnt lgkmcnt(4)
	v_mfma_f32_32x32x16_bf16 v[84:99], v[216:219], v[112:115], v[84:99]
	s_waitcnt lgkmcnt(3)
	v_mfma_f32_32x32x16_bf16 v[68:83], v[220:223], v[120:123], v[68:83]
	s_waitcnt lgkmcnt(2)
	v_mfma_f32_32x32x16_bf16 v[84:99], v[224:227], v[120:123], v[84:99]
	s_waitcnt lgkmcnt(1)
	v_mfma_f32_32x32x16_bf16 v[68:83], v[228:231], v[128:131], v[68:83]
	s_waitcnt lgkmcnt(0)
	s_nop 0
	v_mfma_f32_32x32x16_bf16 v[84:99], v[232:235], v[128:131], v[84:99]
	s_cbranch_scc1 .LBB0_1880
	v_sub_u32_e32 v1, v1, v137
	v_cmp_lt_i32_e32 vcc, 0, v1
	s_nop 5
	v_cndmask_b32_e32 v68, v168, v68, vcc
	v_cmp_lt_i32_e32 vcc, 32, v1
	s_nop 1
	v_cndmask_b32_e32 v84, v168, v84, vcc
	v_cmp_lt_i32_e32 vcc, 1, v1
	s_nop 1
	v_cndmask_b32_e32 v69, v168, v69, vcc
	v_cmp_lt_i32_e32 vcc, 33, v1
	s_nop 1
	v_cndmask_b32_e32 v85, v168, v85, vcc
	v_cmp_lt_i32_e32 vcc, 2, v1
	s_nop 1
	v_cndmask_b32_e32 v70, v168, v70, vcc
	v_cmp_lt_i32_e32 vcc, 34, v1
	s_nop 1
	v_cndmask_b32_e32 v86, v168, v86, vcc
	v_cmp_lt_i32_e32 vcc, 3, v1
	s_nop 1
	v_cndmask_b32_e32 v71, v168, v71, vcc
	v_cmp_lt_i32_e32 vcc, 35, v1
	s_nop 1
	v_cndmask_b32_e32 v87, v168, v87, vcc
	v_cmp_lt_i32_e32 vcc, 8, v1
	s_nop 1
	v_cndmask_b32_e32 v72, v168, v72, vcc
	v_cmp_lt_i32_e32 vcc, 40, v1
	s_nop 1
	v_cndmask_b32_e32 v88, v168, v88, vcc
	v_cmp_lt_i32_e32 vcc, 9, v1
	s_nop 1
	v_cndmask_b32_e32 v73, v168, v73, vcc
	v_cmp_lt_i32_e32 vcc, 41, v1
	s_nop 1
	v_cndmask_b32_e32 v89, v168, v89, vcc
	v_cmp_lt_i32_e32 vcc, 10, v1
	s_nop 1
	v_cndmask_b32_e32 v74, v168, v74, vcc
	v_cmp_lt_i32_e32 vcc, 42, v1
	s_nop 1
	v_cndmask_b32_e32 v90, v168, v90, vcc
	v_cmp_lt_i32_e32 vcc, 11, v1
	s_nop 1
	v_cndmask_b32_e32 v75, v168, v75, vcc
	v_cmp_lt_i32_e32 vcc, 43, v1
	s_nop 1
	v_cndmask_b32_e32 v91, v168, v91, vcc
	v_cmp_lt_i32_e32 vcc, 16, v1
	s_nop 1
	v_cndmask_b32_e32 v76, v168, v76, vcc
	v_cmp_lt_i32_e32 vcc, 48, v1
	s_nop 1
	v_cndmask_b32_e32 v92, v168, v92, vcc
	v_cmp_lt_i32_e32 vcc, 17, v1
	s_nop 1
	v_cndmask_b32_e32 v77, v168, v77, vcc
	v_cmp_lt_i32_e32 vcc, 49, v1
	s_nop 1
	v_cndmask_b32_e32 v93, v168, v93, vcc
	v_cmp_lt_i32_e32 vcc, 18, v1
	s_nop 1
	v_cndmask_b32_e32 v78, v168, v78, vcc
	v_cmp_lt_i32_e32 vcc, 50, v1
	s_nop 1
	v_cndmask_b32_e32 v94, v168, v94, vcc
	v_cmp_lt_i32_e32 vcc, 19, v1
	s_nop 1
	v_cndmask_b32_e32 v79, v168, v79, vcc
	v_cmp_lt_i32_e32 vcc, 51, v1
	s_nop 1
	v_cndmask_b32_e32 v95, v168, v95, vcc
	v_cmp_lt_i32_e32 vcc, 24, v1
	s_nop 1
	v_cndmask_b32_e32 v80, v168, v80, vcc
	v_cmp_lt_i32_e32 vcc, 56, v1
	s_nop 1
	v_cndmask_b32_e32 v96, v168, v96, vcc
	v_cmp_lt_i32_e32 vcc, 25, v1
	s_nop 1
	v_cndmask_b32_e32 v81, v168, v81, vcc
	v_cmp_lt_i32_e32 vcc, 57, v1
	s_nop 1
	v_cndmask_b32_e32 v97, v168, v97, vcc
	v_cmp_lt_i32_e32 vcc, 26, v1
	s_nop 1
	v_cndmask_b32_e32 v82, v168, v82, vcc
	v_cmp_lt_i32_e32 vcc, 58, v1
	s_nop 1
	v_cndmask_b32_e32 v98, v168, v98, vcc
	v_cmp_lt_i32_e32 vcc, 27, v1
	s_nop 1
	v_cndmask_b32_e32 v83, v168, v83, vcc
	v_cmp_lt_i32_e32 vcc, 59, v1
	s_nop 1
	v_cndmask_b32_e32 v99, v168, v99, vcc
